# split V part hand-written: 8 row loads issued together, 16 LDS byte reads per gather issued together (on top of LDS-staged topk score tile)
# speedup vs baseline: 1.0104x; 1.0104x over previous
.Lcv_end:
.LBB0_414:
	s_cmpk_gt_i32 s6, 0x10f
	s_cbranch_scc1 .LBB0_449
	s_waitcnt vmcnt(0)
	v_readfirstlane_b32 s16, v0
	v_readlane_b32 s44, v252, 43
	v_readlane_b32 s45, v252, 44
	v_readlane_b32 s46, v254, 0
	v_readlane_b32 s47, v254, 1
	s_lshr_b32 s16, s16, 6
	v_and_b32_e32 v32, 63, v0
	v_lshlrev_b32_e32 v32, 3, v32
	s_lshl_b32 s17, s16, 12
	v_add_u32_e32 v33, s17, v32
	v_and_b32_e32 v34, 0x7f, v0
	v_bfe_u32 v22, v0, 7, 1
	v_bfe_u32 v23, v0, 8, 1
	v_lshl_add_u32 v24, v23, 1, v22
	v_bfe_u32 v25, v34, 2, 2
	v_xor_b32_e32 v24, v24, v25
	v_lshlrev_b32_e32 v24, 4, v24
	v_lshl_add_u32 v35, v34, 6, v24
	v_lshl_add_u32 v34, v22, 14, v34
	v_lshl_add_u32 v34, v23, 11, v34
	s_lshl_b32 s17, s16, 3
.Lvp_tile:
	s_mul_hi_u32 s8, s6, 0x78787879
	s_lshr_b32 s8, s8, 5
	s_mul_i32 s9, s8, 68
	s_sub_u32 s9, s6, s9
	s_lshl_b32 s9, s9, 6
	s_add_u32 s9, s9, s17
	s_lshl_b32 s10, s8, 12
	s_add_u32 s10, s10, s9
	s_lshl_b32 s11, s8, 8
	s_add_u32 s11, s11, s9
	s_add_u32 s11, s11, 0x3000
	s_cmp_lt_u32 s9, 0x1000
	s_cselect_b32 s10, s10, s11
	s_mul_hi_u32 s11, s10, 0x3400
	s_mul_i32 s10, s10, 0x3400
	s_add_u32 s48, s44, s10
	s_addc_u32 s49, s45, s11
	global_load_dwordx2 v[6:7], v32, s[48:49] offset:2560 nt
	s_add_u32 s48, s48, 0x3400
	s_addc_u32 s49, s49, 0
	global_load_dwordx2 v[8:9], v32, s[48:49] offset:2560 nt
	s_add_u32 s48, s48, 0x3400
	s_addc_u32 s49, s49, 0
	global_load_dwordx2 v[10:11], v32, s[48:49] offset:2560 nt
	s_add_u32 s48, s48, 0x3400
	s_addc_u32 s49, s49, 0
	global_load_dwordx2 v[12:13], v32, s[48:49] offset:2560 nt
	s_add_u32 s48, s48, 0x3400
	s_addc_u32 s49, s49, 0
	global_load_dwordx2 v[14:15], v32, s[48:49] offset:2560 nt
	s_add_u32 s48, s48, 0x3400
	s_addc_u32 s49, s49, 0
	global_load_dwordx2 v[16:17], v32, s[48:49] offset:2560 nt
	s_add_u32 s48, s48, 0x3400
	s_addc_u32 s49, s49, 0
	global_load_dwordx2 v[18:19], v32, s[48:49] offset:2560 nt
	s_add_u32 s48, s48, 0x3400
	s_addc_u32 s49, s49, 0
	global_load_dwordx2 v[20:21], v32, s[48:49] offset:2560 nt
	s_lshl_b32 s10, s6, 15
	s_add_u32 s50, s46, s10
	s_addc_u32 s51, s47, 0
	s_waitcnt vmcnt(7)
	v_cvt_pk_f32_fp8_e32 v[22:23], v6
	v_cvt_pk_f32_fp8_sdwa v[24:25], v6 src0_sel:WORD_1
	v_cvt_pk_f32_fp8_e32 v[26:27], v7
	v_cvt_pk_f32_fp8_sdwa v[28:29], v7 src0_sel:WORD_1
	v_pk_mul_f32 v[22:23], v[22:23], 2.0 op_sel_hi:[1,0]
	v_pk_mul_f32 v[24:25], v[24:25], 2.0 op_sel_hi:[1,0]
	v_pk_mul_f32 v[26:27], v[26:27], 2.0 op_sel_hi:[1,0]
	v_pk_mul_f32 v[28:29], v[28:29], 2.0 op_sel_hi:[1,0]
	v_med3_f32 v22, v22, s79, v204
	v_med3_f32 v23, v23, s79, v204
	v_med3_f32 v24, v24, s79, v204
	v_med3_f32 v25, v25, s79, v204
	v_med3_f32 v26, v26, s79, v204
	v_med3_f32 v27, v27, s79, v204
	v_med3_f32 v28, v28, s79, v204
	v_med3_f32 v29, v29, s79, v204
	v_cvt_pk_fp8_f32 v30, v22, v23
	v_cvt_pk_fp8_f32 v31, v26, v27
	v_cvt_pk_fp8_f32 v30, v24, v25 op_sel:[0,0,1]
	v_cvt_pk_fp8_f32 v31, v28, v29 op_sel:[0,0,1]
	ds_write_b64 v33, v[30:31]
	s_waitcnt vmcnt(6)
	v_cvt_pk_f32_fp8_e32 v[22:23], v8
	v_cvt_pk_f32_fp8_sdwa v[24:25], v8 src0_sel:WORD_1
	v_cvt_pk_f32_fp8_e32 v[26:27], v9
	v_cvt_pk_f32_fp8_sdwa v[28:29], v9 src0_sel:WORD_1
	v_pk_mul_f32 v[22:23], v[22:23], 2.0 op_sel_hi:[1,0]
	v_pk_mul_f32 v[24:25], v[24:25], 2.0 op_sel_hi:[1,0]
	v_pk_mul_f32 v[26:27], v[26:27], 2.0 op_sel_hi:[1,0]
	v_pk_mul_f32 v[28:29], v[28:29], 2.0 op_sel_hi:[1,0]
	v_med3_f32 v22, v22, s79, v204
	v_med3_f32 v23, v23, s79, v204
	v_med3_f32 v24, v24, s79, v204
	v_med3_f32 v25, v25, s79, v204
	v_med3_f32 v26, v26, s79, v204
	v_med3_f32 v27, v27, s79, v204
	v_med3_f32 v28, v28, s79, v204
	v_med3_f32 v29, v29, s79, v204
	v_cvt_pk_fp8_f32 v30, v22, v23
	v_cvt_pk_fp8_f32 v31, v26, v27
	v_cvt_pk_fp8_f32 v30, v24, v25 op_sel:[0,0,1]
	v_cvt_pk_fp8_f32 v31, v28, v29 op_sel:[0,0,1]
	ds_write_b64 v33, v[30:31] offset:512
	s_waitcnt vmcnt(5)
	v_cvt_pk_f32_fp8_e32 v[22:23], v10
	v_cvt_pk_f32_fp8_sdwa v[24:25], v10 src0_sel:WORD_1
	v_cvt_pk_f32_fp8_e32 v[26:27], v11
	v_cvt_pk_f32_fp8_sdwa v[28:29], v11 src0_sel:WORD_1
	v_pk_mul_f32 v[22:23], v[22:23], 2.0 op_sel_hi:[1,0]
	v_pk_mul_f32 v[24:25], v[24:25], 2.0 op_sel_hi:[1,0]
	v_pk_mul_f32 v[26:27], v[26:27], 2.0 op_sel_hi:[1,0]
	v_pk_mul_f32 v[28:29], v[28:29], 2.0 op_sel_hi:[1,0]
	v_med3_f32 v22, v22, s79, v204
	v_med3_f32 v23, v23, s79, v204
	v_med3_f32 v24, v24, s79, v204
	v_med3_f32 v25, v25, s79, v204
	v_med3_f32 v26, v26, s79, v204
	v_med3_f32 v27, v27, s79, v204
	v_med3_f32 v28, v28, s79, v204
	v_med3_f32 v29, v29, s79, v204
	v_cvt_pk_fp8_f32 v30, v22, v23
	v_cvt_pk_fp8_f32 v31, v26, v27
	v_cvt_pk_fp8_f32 v30, v24, v25 op_sel:[0,0,1]
	v_cvt_pk_fp8_f32 v31, v28, v29 op_sel:[0,0,1]
	ds_write_b64 v33, v[30:31] offset:1024
	s_waitcnt vmcnt(4)
	v_cvt_pk_f32_fp8_e32 v[22:23], v12
	v_cvt_pk_f32_fp8_sdwa v[24:25], v12 src0_sel:WORD_1
	v_cvt_pk_f32_fp8_e32 v[26:27], v13
	v_cvt_pk_f32_fp8_sdwa v[28:29], v13 src0_sel:WORD_1
	v_pk_mul_f32 v[22:23], v[22:23], 2.0 op_sel_hi:[1,0]
	v_pk_mul_f32 v[24:25], v[24:25], 2.0 op_sel_hi:[1,0]
	v_pk_mul_f32 v[26:27], v[26:27], 2.0 op_sel_hi:[1,0]
	v_pk_mul_f32 v[28:29], v[28:29], 2.0 op_sel_hi:[1,0]
	v_med3_f32 v22, v22, s79, v204
	v_med3_f32 v23, v23, s79, v204
	v_med3_f32 v24, v24, s79, v204
	v_med3_f32 v25, v25, s79, v204
	v_med3_f32 v26, v26, s79, v204
	v_med3_f32 v27, v27, s79, v204
	v_med3_f32 v28, v28, s79, v204
	v_med3_f32 v29, v29, s79, v204
	v_cvt_pk_fp8_f32 v30, v22, v23
	v_cvt_pk_fp8_f32 v31, v26, v27
	v_cvt_pk_fp8_f32 v30, v24, v25 op_sel:[0,0,1]
	v_cvt_pk_fp8_f32 v31, v28, v29 op_sel:[0,0,1]
	ds_write_b64 v33, v[30:31] offset:1536
	s_waitcnt vmcnt(3)
	v_cvt_pk_f32_fp8_e32 v[22:23], v14
	v_cvt_pk_f32_fp8_sdwa v[24:25], v14 src0_sel:WORD_1
	v_cvt_pk_f32_fp8_e32 v[26:27], v15
	v_cvt_pk_f32_fp8_sdwa v[28:29], v15 src0_sel:WORD_1
	v_pk_mul_f32 v[22:23], v[22:23], 2.0 op_sel_hi:[1,0]
	v_pk_mul_f32 v[24:25], v[24:25], 2.0 op_sel_hi:[1,0]
	v_pk_mul_f32 v[26:27], v[26:27], 2.0 op_sel_hi:[1,0]
	v_pk_mul_f32 v[28:29], v[28:29], 2.0 op_sel_hi:[1,0]
	v_med3_f32 v22, v22, s79, v204
	v_med3_f32 v23, v23, s79, v204
	v_med3_f32 v24, v24, s79, v204
	v_med3_f32 v25, v25, s79, v204
	v_med3_f32 v26, v26, s79, v204
	v_med3_f32 v27, v27, s79, v204
	v_med3_f32 v28, v28, s79, v204
	v_med3_f32 v29, v29, s79, v204
	v_cvt_pk_fp8_f32 v30, v22, v23
	v_cvt_pk_fp8_f32 v31, v26, v27
	v_cvt_pk_fp8_f32 v30, v24, v25 op_sel:[0,0,1]
	v_cvt_pk_fp8_f32 v31, v28, v29 op_sel:[0,0,1]
	ds_write_b64 v33, v[30:31] offset:2048
	s_waitcnt vmcnt(2)
	v_cvt_pk_f32_fp8_e32 v[22:23], v16
	v_cvt_pk_f32_fp8_sdwa v[24:25], v16 src0_sel:WORD_1
	v_cvt_pk_f32_fp8_e32 v[26:27], v17
	v_cvt_pk_f32_fp8_sdwa v[28:29], v17 src0_sel:WORD_1
	v_pk_mul_f32 v[22:23], v[22:23], 2.0 op_sel_hi:[1,0]
	v_pk_mul_f32 v[24:25], v[24:25], 2.0 op_sel_hi:[1,0]
	v_pk_mul_f32 v[26:27], v[26:27], 2.0 op_sel_hi:[1,0]
	v_pk_mul_f32 v[28:29], v[28:29], 2.0 op_sel_hi:[1,0]
	v_med3_f32 v22, v22, s79, v204
	v_med3_f32 v23, v23, s79, v204
	v_med3_f32 v24, v24, s79, v204
	v_med3_f32 v25, v25, s79, v204
	v_med3_f32 v26, v26, s79, v204
	v_med3_f32 v27, v27, s79, v204
	v_med3_f32 v28, v28, s79, v204
	v_med3_f32 v29, v29, s79, v204
	v_cvt_pk_fp8_f32 v30, v22, v23
	v_cvt_pk_fp8_f32 v31, v26, v27
	v_cvt_pk_fp8_f32 v30, v24, v25 op_sel:[0,0,1]
	v_cvt_pk_fp8_f32 v31, v28, v29 op_sel:[0,0,1]
	ds_write_b64 v33, v[30:31] offset:2560
	s_waitcnt vmcnt(1)
	v_cvt_pk_f32_fp8_e32 v[22:23], v18
	v_cvt_pk_f32_fp8_sdwa v[24:25], v18 src0_sel:WORD_1
	v_cvt_pk_f32_fp8_e32 v[26:27], v19
	v_cvt_pk_f32_fp8_sdwa v[28:29], v19 src0_sel:WORD_1
	v_pk_mul_f32 v[22:23], v[22:23], 2.0 op_sel_hi:[1,0]
	v_pk_mul_f32 v[24:25], v[24:25], 2.0 op_sel_hi:[1,0]
	v_pk_mul_f32 v[26:27], v[26:27], 2.0 op_sel_hi:[1,0]
	v_pk_mul_f32 v[28:29], v[28:29], 2.0 op_sel_hi:[1,0]
	v_med3_f32 v22, v22, s79, v204
	v_med3_f32 v23, v23, s79, v204
	v_med3_f32 v24, v24, s79, v204
	v_med3_f32 v25, v25, s79, v204
	v_med3_f32 v26, v26, s79, v204
	v_med3_f32 v27, v27, s79, v204
	v_med3_f32 v28, v28, s79, v204
	v_med3_f32 v29, v29, s79, v204
	v_cvt_pk_fp8_f32 v30, v22, v23
	v_cvt_pk_fp8_f32 v31, v26, v27
	v_cvt_pk_fp8_f32 v30, v24, v25 op_sel:[0,0,1]
	v_cvt_pk_fp8_f32 v31, v28, v29 op_sel:[0,0,1]
	ds_write_b64 v33, v[30:31] offset:3072
	s_waitcnt vmcnt(0)
	v_cvt_pk_f32_fp8_e32 v[22:23], v20
	v_cvt_pk_f32_fp8_sdwa v[24:25], v20 src0_sel:WORD_1
	v_cvt_pk_f32_fp8_e32 v[26:27], v21
	v_cvt_pk_f32_fp8_sdwa v[28:29], v21 src0_sel:WORD_1
	v_pk_mul_f32 v[22:23], v[22:23], 2.0 op_sel_hi:[1,0]
	v_pk_mul_f32 v[24:25], v[24:25], 2.0 op_sel_hi:[1,0]
	v_pk_mul_f32 v[26:27], v[26:27], 2.0 op_sel_hi:[1,0]
	v_pk_mul_f32 v[28:29], v[28:29], 2.0 op_sel_hi:[1,0]
	v_med3_f32 v22, v22, s79, v204
	v_med3_f32 v23, v23, s79, v204
	v_med3_f32 v24, v24, s79, v204
	v_med3_f32 v25, v25, s79, v204
	v_med3_f32 v26, v26, s79, v204
	v_med3_f32 v27, v27, s79, v204
	v_med3_f32 v28, v28, s79, v204
	v_med3_f32 v29, v29, s79, v204
	v_cvt_pk_fp8_f32 v30, v22, v23
	v_cvt_pk_fp8_f32 v31, v26, v27
	v_cvt_pk_fp8_f32 v30, v24, v25 op_sel:[0,0,1]
	v_cvt_pk_fp8_f32 v31, v28, v29 op_sel:[0,0,1]
	ds_write_b64 v33, v[30:31] offset:3584
	s_waitcnt lgkmcnt(0)
	s_barrier
	ds_read_u8 v36, v34
	ds_read_u8 v37, v34 offset:512
	ds_read_u8 v38, v34 offset:1024
	ds_read_u8 v39, v34 offset:1536
	ds_read_u8 v40, v34 offset:4096
	ds_read_u8 v41, v34 offset:4608
	ds_read_u8 v42, v34 offset:5120
	ds_read_u8 v43, v34 offset:5632
	ds_read_u8 v44, v34 offset:8192
	ds_read_u8 v45, v34 offset:8704
	ds_read_u8 v46, v34 offset:9216
	ds_read_u8 v47, v34 offset:9728
	ds_read_u8 v48, v34 offset:12288
	ds_read_u8 v49, v34 offset:12800
	ds_read_u8 v50, v34 offset:13312
	ds_read_u8 v51, v34 offset:13824
	s_waitcnt lgkmcnt(12)
	v_lshl_or_b32 v52, v39, 8, v38
	v_lshl_or_b32 v52, v52, 8, v37
	v_lshl_or_b32 v52, v52, 8, v36
	s_waitcnt lgkmcnt(8)
	v_lshl_or_b32 v53, v43, 8, v42
	v_lshl_or_b32 v53, v53, 8, v41
	v_lshl_or_b32 v53, v53, 8, v40
	s_waitcnt lgkmcnt(4)
	v_lshl_or_b32 v54, v47, 8, v46
	v_lshl_or_b32 v54, v54, 8, v45
	v_lshl_or_b32 v54, v54, 8, v44
	s_waitcnt lgkmcnt(0)
	v_lshl_or_b32 v55, v51, 8, v50
	v_lshl_or_b32 v55, v55, 8, v49
	v_lshl_or_b32 v55, v55, 8, v48
	global_store_dwordx4 v35, v[52:55], s[50:51]
	s_add_u32 s50, s50, 0x2000
	s_addc_u32 s51, s51, 0
	s_nop 0
	ds_read_u8 v36, v34 offset:128
	ds_read_u8 v37, v34 offset:640
	ds_read_u8 v38, v34 offset:1152
	ds_read_u8 v39, v34 offset:1664
	ds_read_u8 v40, v34 offset:4224
	ds_read_u8 v41, v34 offset:4736
	ds_read_u8 v42, v34 offset:5248
	ds_read_u8 v43, v34 offset:5760
	ds_read_u8 v44, v34 offset:8320
	ds_read_u8 v45, v34 offset:8832
	ds_read_u8 v46, v34 offset:9344
	ds_read_u8 v47, v34 offset:9856
	ds_read_u8 v48, v34 offset:12416
	ds_read_u8 v49, v34 offset:12928
	ds_read_u8 v50, v34 offset:13440
	ds_read_u8 v51, v34 offset:13952
	s_waitcnt lgkmcnt(12)
	v_lshl_or_b32 v52, v39, 8, v38
	v_lshl_or_b32 v52, v52, 8, v37
	v_lshl_or_b32 v52, v52, 8, v36
	s_waitcnt lgkmcnt(8)
	v_lshl_or_b32 v53, v43, 8, v42
	v_lshl_or_b32 v53, v53, 8, v41
	v_lshl_or_b32 v53, v53, 8, v40
	s_waitcnt lgkmcnt(4)
	v_lshl_or_b32 v54, v47, 8, v46
	v_lshl_or_b32 v54, v54, 8, v45
	v_lshl_or_b32 v54, v54, 8, v44
	s_waitcnt lgkmcnt(0)
	v_lshl_or_b32 v55, v51, 8, v50
	v_lshl_or_b32 v55, v55, 8, v49
	v_lshl_or_b32 v55, v55, 8, v48
	global_store_dwordx4 v35, v[52:55], s[50:51]
	s_add_u32 s50, s50, 0x2000
	s_addc_u32 s51, s51, 0
	s_nop 0
	ds_read_u8 v36, v34 offset:256
	ds_read_u8 v37, v34 offset:768
	ds_read_u8 v38, v34 offset:1280
	ds_read_u8 v39, v34 offset:1792
	ds_read_u8 v40, v34 offset:4352
	ds_read_u8 v41, v34 offset:4864
	ds_read_u8 v42, v34 offset:5376
	ds_read_u8 v43, v34 offset:5888
	ds_read_u8 v44, v34 offset:8448
	ds_read_u8 v45, v34 offset:8960
	ds_read_u8 v46, v34 offset:9472
	ds_read_u8 v47, v34 offset:9984
	ds_read_u8 v48, v34 offset:12544
	ds_read_u8 v49, v34 offset:13056
	ds_read_u8 v50, v34 offset:13568
	ds_read_u8 v51, v34 offset:14080
	s_waitcnt lgkmcnt(12)
	v_lshl_or_b32 v52, v39, 8, v38
	v_lshl_or_b32 v52, v52, 8, v37
	v_lshl_or_b32 v52, v52, 8, v36
	s_waitcnt lgkmcnt(8)
	v_lshl_or_b32 v53, v43, 8, v42
	v_lshl_or_b32 v53, v53, 8, v41
	v_lshl_or_b32 v53, v53, 8, v40
	s_waitcnt lgkmcnt(4)
	v_lshl_or_b32 v54, v47, 8, v46
	v_lshl_or_b32 v54, v54, 8, v45
	v_lshl_or_b32 v54, v54, 8, v44
	s_waitcnt lgkmcnt(0)
	v_lshl_or_b32 v55, v51, 8, v50
	v_lshl_or_b32 v55, v55, 8, v49
	v_lshl_or_b32 v55, v55, 8, v48
	global_store_dwordx4 v35, v[52:55], s[50:51]
	s_add_u32 s50, s50, 0x2000
	s_addc_u32 s51, s51, 0
	s_nop 0
	ds_read_u8 v36, v34 offset:384
	ds_read_u8 v37, v34 offset:896
	ds_read_u8 v38, v34 offset:1408
	ds_read_u8 v39, v34 offset:1920
	ds_read_u8 v40, v34 offset:4480
	ds_read_u8 v41, v34 offset:4992
	ds_read_u8 v42, v34 offset:5504
	ds_read_u8 v43, v34 offset:6016
	ds_read_u8 v44, v34 offset:8576
	ds_read_u8 v45, v34 offset:9088
	ds_read_u8 v46, v34 offset:9600
	ds_read_u8 v47, v34 offset:10112
	ds_read_u8 v48, v34 offset:12672
	ds_read_u8 v49, v34 offset:13184
	ds_read_u8 v50, v34 offset:13696
	ds_read_u8 v51, v34 offset:14208
	s_waitcnt lgkmcnt(12)
	v_lshl_or_b32 v52, v39, 8, v38
	v_lshl_or_b32 v52, v52, 8, v37
	v_lshl_or_b32 v52, v52, 8, v36
	s_waitcnt lgkmcnt(8)
	v_lshl_or_b32 v53, v43, 8, v42
	v_lshl_or_b32 v53, v53, 8, v41
	v_lshl_or_b32 v53, v53, 8, v40
	s_waitcnt lgkmcnt(4)
	v_lshl_or_b32 v54, v47, 8, v46
	v_lshl_or_b32 v54, v54, 8, v45
	v_lshl_or_b32 v54, v54, 8, v44
	s_waitcnt lgkmcnt(0)
	v_lshl_or_b32 v55, v51, 8, v50
	v_lshl_or_b32 v55, v55, 8, v49
	v_lshl_or_b32 v55, v55, 8, v48
	global_store_dwordx4 v35, v[52:55], s[50:51]
	s_add_u32 s6, s6, s82
	s_waitcnt lgkmcnt(0)
	s_barrier
	s_cmp_lt_u32 s6, 0x110
	s_cbranch_scc1 .Lvp_tile
